# v37 + fp8 GEMM K-loops: LDS-DMA loads use SGPR base + 32-bit VGPR offset (+128 imm with M0 compensated) instead of 16 64-bit VALU address adds per trip
# baseline (speedup 1.0000x reference)
.LBB0_177:
	s_add_u32 s28, s4, s26
	s_addc_u32 s29, s5, s27
	s_add_u32 s30, s28, 0xe000100
	s_addc_u32 s31, s29, 0
	ds_read_b128 v[24:27], v252
	ds_read_b128 v[28:31], v253
	s_and_b64 s[28:29], s[34:35], exec
	ds_read_b128 v[16:19], v252 offset:2048
	ds_read_b128 v[20:23], v253 offset:2048
	s_cselect_b32 s29, s7, s31
	s_cselect_b32 s28, s6, s30
	s_add_u32 s61, s56, s26
	ds_read_b128 v[8:11], v252 offset:16384
	ds_read_b128 v[12:15], v253 offset:16384
	s_addc_u32 s62, s57, s27
	ds_read_b128 v[0:3], v252 offset:18432
	ds_read_b128 v[4:7], v253 offset:18432
	s_and_b64 s[30:31], s[34:35], exec
	s_cselect_b32 s31, s23, s62
	s_cselect_b32 s30, s22, s61
	s_add_u32 s61, s58, s26
	s_addc_u32 s62, s59, s27
	s_and_b64 s[34:35], s[34:35], exec
	s_cselect_b32 s35, s25, s62
	s_cselect_b32 s34, s24, s61
	s_add_u32 s100, s16, s26
	s_addc_u32 s101, s17, s27
	s_add_i32 m0, s37, 0xc000
	ds_read_b128 v[186:189], v206
	ds_read_b128 v[214:217], v206 offset:2048
	ds_read_b128 v[190:193], v207
	ds_read_b128 v[218:221], v207 offset:2048
	ds_read_b128 v[222:225], v206 offset:4096
	ds_read_b128 v[230:233], v206 offset:6144
	ds_read_b128 v[226:229], v207 offset:4096
	ds_read_b128 v[234:237], v207 offset:6144
	global_load_lds_dwordx4 v166, s[100:101]
	s_add_i32 m0, s37, 0xe000
	s_nop 0
	global_load_lds_dwordx4 v168, s[100:101]
	s_waitcnt vmcnt(8)
	s_waitcnt lgkmcnt(0)
	s_barrier
	s_setprio 1
	s_waitcnt lgkmcnt(0)
	v_mfma_f32_16x16x128_f8f6f4 v[156:159], v[24:31], v[186:193], v[156:159]
	v_mfma_f32_16x16x128_f8f6f4 v[152:155], v[16:23], v[186:193], v[152:155]
	v_mfma_f32_16x16x128_f8f6f4 v[144:147], v[24:31], v[214:221], v[144:147]
	v_mfma_f32_16x16x128_f8f6f4 v[136:139], v[16:23], v[214:221], v[136:139]
	v_mfma_f32_16x16x128_f8f6f4 v[128:131], v[24:31], v[222:229], v[128:131]
	v_mfma_f32_16x16x128_f8f6f4 v[120:123], v[16:23], v[222:229], v[120:123]
	v_mfma_f32_16x16x128_f8f6f4 v[112:115], v[24:31], v[230:237], v[112:115]
	v_mfma_f32_16x16x128_f8f6f4 v[104:107], v[16:23], v[230:237], v[104:107]
	v_mfma_f32_16x16x128_f8f6f4 v[148:151], v[8:15], v[186:193], v[148:151]
	v_mfma_f32_16x16x128_f8f6f4 v[140:143], v[0:7], v[186:193], v[140:143]
	v_mfma_f32_16x16x128_f8f6f4 v[132:135], v[8:15], v[214:221], v[132:135]
	v_mfma_f32_16x16x128_f8f6f4 v[124:127], v[0:7], v[214:221], v[124:127]
	v_mfma_f32_16x16x128_f8f6f4 v[116:119], v[8:15], v[222:229], v[116:119]
	v_mfma_f32_16x16x128_f8f6f4 v[108:111], v[0:7], v[222:229], v[108:111]
	v_mfma_f32_16x16x128_f8f6f4 v[100:103], v[8:15], v[230:237], v[100:103]
	v_mfma_f32_16x16x128_f8f6f4 v[96:99], v[0:7], v[230:237], v[96:99]
	s_setprio 0
	s_barrier
	s_add_i32 s61, s44, s36
	s_mov_b32 m0, s61
	ds_read_b128 v[214:217], v206 offset:16384
	ds_read_b128 v[222:225], v206 offset:18432
	ds_read_b128 v[218:221], v207 offset:16384
	ds_read_b128 v[226:229], v207 offset:18432
	ds_read_b128 v[230:233], v206 offset:20480
	ds_read_b128 v[238:241], v206 offset:22528
	ds_read_b128 v[234:237], v207 offset:20480
	ds_read_b128 v[242:245], v207 offset:22528
	global_load_lds_dwordx4 v160, s[30:31]
	s_add_i32 m0, s61, 0x2000
	s_add_i32 s98, s46, s36
	global_load_lds_dwordx4 v162, s[30:31]
	s_mov_b32 m0, s98
	s_nop 0
	global_load_lds_dwordx4 v160, s[34:35]
	s_add_i32 m0, s98, 0x2000
	v_mov_b32_e32 v173, v165
	global_load_lds_dwordx4 v162, s[34:35]
	s_mov_b32 m0, s37
	s_nop 0
	global_load_lds_dwordx4 v164, s[28:29]
	s_mov_b32 m0, s38
	s_nop 0
	global_load_lds_dwordx4 v172, s[28:29]
	s_waitcnt vmcnt(8)
	s_waitcnt lgkmcnt(0)
	s_barrier
	s_setprio 1
	s_waitcnt lgkmcnt(0)
	v_mfma_f32_16x16x128_f8f6f4 v[92:95], v[24:31], v[214:221], v[92:95]
	v_mfma_f32_16x16x128_f8f6f4 v[88:91], v[16:23], v[214:221], v[88:91]
	v_mfma_f32_16x16x128_f8f6f4 v[80:83], v[24:31], v[222:229], v[80:83]
	v_mfma_f32_16x16x128_f8f6f4 v[72:75], v[16:23], v[222:229], v[72:75]
	v_mfma_f32_16x16x128_f8f6f4 v[64:67], v[24:31], v[230:237], v[64:67]
	v_mfma_f32_16x16x128_f8f6f4 v[56:59], v[16:23], v[230:237], v[56:59]
	v_mfma_f32_16x16x128_f8f6f4 v[48:51], v[24:31], v[238:245], v[48:51]
	v_mfma_f32_16x16x128_f8f6f4 v[40:43], v[16:23], v[238:245], v[40:43]
	v_mfma_f32_16x16x128_f8f6f4 v[84:87], v[8:15], v[214:221], v[84:87]
	v_mfma_f32_16x16x128_f8f6f4 v[76:79], v[0:7], v[214:221], v[76:79]
	v_mfma_f32_16x16x128_f8f6f4 v[68:71], v[8:15], v[222:229], v[68:71]
	v_mfma_f32_16x16x128_f8f6f4 v[60:63], v[0:7], v[222:229], v[60:63]
	v_mfma_f32_16x16x128_f8f6f4 v[52:55], v[8:15], v[230:237], v[52:55]
	v_mfma_f32_16x16x128_f8f6f4 v[44:47], v[0:7], v[230:237], v[44:47]
	v_mfma_f32_16x16x128_f8f6f4 v[36:39], v[8:15], v[238:245], v[36:39]
	v_mfma_f32_16x16x128_f8f6f4 v[32:35], v[0:7], v[238:245], v[32:35]
	s_setprio 0
	s_barrier
	ds_read_b128 v[0:3], v252 offset:32768
	ds_read_b128 v[4:7], v253 offset:32768
	ds_read_b128 v[8:11], v252 offset:34816
	ds_read_b128 v[12:15], v253 offset:34816
	ds_read_b128 v[16:19], v252 offset:49152
	ds_read_b128 v[20:23], v253 offset:49152
	ds_read_b128 v[24:27], v252 offset:51200
	ds_read_b128 v[28:31], v253 offset:51200
	s_mov_b32 m0, s39
	ds_read_b128 v[214:217], v206 offset:32768
	ds_read_b128 v[222:225], v206 offset:34816
	ds_read_b128 v[218:221], v207 offset:32768
	ds_read_b128 v[226:229], v207 offset:34816
	ds_read_b128 v[230:233], v206 offset:36864
	ds_read_b128 v[238:241], v206 offset:38912
	ds_read_b128 v[234:237], v207 offset:36864
	ds_read_b128 v[242:245], v207 offset:38912
	global_load_lds_dwordx4 v184, s[28:29]
	s_mov_b32 m0, s40
	s_nop 0
	global_load_lds_dwordx4 v182, s[28:29]
	s_waitcnt vmcnt(8)
	s_waitcnt lgkmcnt(0)
	s_barrier
	s_setprio 1
	s_waitcnt lgkmcnt(0)
	v_mfma_f32_16x16x128_f8f6f4 v[156:159], v[0:7], v[214:221], v[156:159]
	v_mfma_f32_16x16x128_f8f6f4 v[152:155], v[8:15], v[214:221], v[152:155]
	v_mfma_f32_16x16x128_f8f6f4 v[144:147], v[0:7], v[222:229], v[144:147]
	v_mfma_f32_16x16x128_f8f6f4 v[136:139], v[8:15], v[222:229], v[136:139]
	v_mfma_f32_16x16x128_f8f6f4 v[128:131], v[0:7], v[230:237], v[128:131]
	v_mfma_f32_16x16x128_f8f6f4 v[120:123], v[8:15], v[230:237], v[120:123]
	v_mfma_f32_16x16x128_f8f6f4 v[112:115], v[0:7], v[238:245], v[112:115]
	v_mfma_f32_16x16x128_f8f6f4 v[104:107], v[8:15], v[238:245], v[104:107]
	v_mfma_f32_16x16x128_f8f6f4 v[148:151], v[16:23], v[214:221], v[148:151]
	v_mfma_f32_16x16x128_f8f6f4 v[140:143], v[24:31], v[214:221], v[140:143]
	v_mfma_f32_16x16x128_f8f6f4 v[132:135], v[16:23], v[222:229], v[132:135]
	v_mfma_f32_16x16x128_f8f6f4 v[124:127], v[24:31], v[222:229], v[124:127]
	v_mfma_f32_16x16x128_f8f6f4 v[116:119], v[16:23], v[230:237], v[116:119]
	v_mfma_f32_16x16x128_f8f6f4 v[108:111], v[24:31], v[230:237], v[108:111]
	v_mfma_f32_16x16x128_f8f6f4 v[100:103], v[16:23], v[238:245], v[100:103]
	v_mfma_f32_16x16x128_f8f6f4 v[96:99], v[24:31], v[238:245], v[96:99]
	s_setprio 0
	s_barrier
	s_add_i32 s99, s36, 0x17f80
	s_mov_b32 m0, s99
	ds_read_b128 v[214:217], v206 offset:49152
	ds_read_b128 v[222:225], v206 offset:51200
	ds_read_b128 v[218:221], v207 offset:49152
	ds_read_b128 v[226:229], v207 offset:51200
	ds_read_b128 v[230:233], v206 offset:53248
	ds_read_b128 v[238:241], v206 offset:55296
	ds_read_b128 v[234:237], v207 offset:53248
	ds_read_b128 v[242:245], v207 offset:55296
	global_load_lds_dwordx4 v160, s[30:31] offset:128
	s_add_i32 m0, s99, 0x2000
	s_add_i32 s99, s36, 0x1bf80
	global_load_lds_dwordx4 v162, s[30:31] offset:128
	s_mov_b32 m0, s99
	s_nop 0
	global_load_lds_dwordx4 v160, s[34:35] offset:128
	s_add_i32 m0, s99, 0x2000
	s_nop 0
	global_load_lds_dwordx4 v162, s[34:35] offset:128
	s_add_i32 m0, s41, 0xffffff80
	s_nop 0
	global_load_lds_dwordx4 v164, s[28:29] offset:128
	s_add_i32 m0, s42, 0xffffff80
	s_nop 0
	global_load_lds_dwordx4 v172, s[28:29] offset:128
	s_waitcnt vmcnt(8)
	s_waitcnt lgkmcnt(0)
	s_barrier
	s_setprio 1
	s_waitcnt lgkmcnt(0)
	v_mfma_f32_16x16x128_f8f6f4 v[92:95], v[0:7], v[214:221], v[92:95]
	v_mfma_f32_16x16x128_f8f6f4 v[88:91], v[8:15], v[214:221], v[88:91]
	v_mfma_f32_16x16x128_f8f6f4 v[80:83], v[0:7], v[222:229], v[80:83]
	v_mfma_f32_16x16x128_f8f6f4 v[72:75], v[8:15], v[222:229], v[72:75]
	v_mfma_f32_16x16x128_f8f6f4 v[64:67], v[0:7], v[230:237], v[64:67]
	v_mfma_f32_16x16x128_f8f6f4 v[56:59], v[8:15], v[230:237], v[56:59]
	v_mfma_f32_16x16x128_f8f6f4 v[48:51], v[0:7], v[238:245], v[48:51]
	v_mfma_f32_16x16x128_f8f6f4 v[40:43], v[8:15], v[238:245], v[40:43]
	v_mfma_f32_16x16x128_f8f6f4 v[84:87], v[16:23], v[214:221], v[84:87]
	v_mfma_f32_16x16x128_f8f6f4 v[76:79], v[24:31], v[214:221], v[76:79]
	v_mfma_f32_16x16x128_f8f6f4 v[68:71], v[16:23], v[222:229], v[68:71]
	v_mfma_f32_16x16x128_f8f6f4 v[60:63], v[24:31], v[222:229], v[60:63]
	v_mfma_f32_16x16x128_f8f6f4 v[52:55], v[16:23], v[230:237], v[52:55]
	v_mfma_f32_16x16x128_f8f6f4 v[44:47], v[24:31], v[230:237], v[44:47]
	v_mfma_f32_16x16x128_f8f6f4 v[36:39], v[16:23], v[238:245], v[36:39]
	v_mfma_f32_16x16x128_f8f6f4 v[32:35], v[24:31], v[238:245], v[32:35]
	s_setprio 0
	s_barrier
	s_add_i32 s60, s60, 2
	s_add_u32 s26, s26, 0x100
	s_addc_u32 s27, s27, 0
	s_cmp_gt_u32 s60, 5
	s_cbranch_scc1 .LBB0_180

.LBB0_590:
	s_add_u32 s36, s8, s4
	s_addc_u32 s37, s9, s5
	s_add_u32 s38, s36, 0xe000100
	s_addc_u32 s39, s37, 0
	ds_read_b128 v[24:27], v252
	ds_read_b128 v[28:31], v253
	s_and_b64 s[36:37], s[40:41], exec
	ds_read_b128 v[16:19], v252 offset:2048
	ds_read_b128 v[20:23], v253 offset:2048
	s_cselect_b32 s37, s11, s39
	s_cselect_b32 s36, s10, s38
	s_add_u32 s90, s27, s4
	ds_read_b128 v[8:11], v252 offset:16384
	ds_read_b128 v[12:15], v253 offset:16384
	s_addc_u32 s91, s86, s5
	ds_read_b128 v[0:3], v252 offset:18432
	ds_read_b128 v[4:7], v253 offset:18432
	s_and_b64 s[38:39], s[40:41], exec
	s_cselect_b32 s39, s29, s91
	s_cselect_b32 s38, s28, s90
	s_add_u32 s90, s87, s4
	s_addc_u32 s91, s88, s5
	s_and_b64 s[40:41], s[40:41], exec
	s_cselect_b32 s41, s31, s91
	s_cselect_b32 s40, s30, s90
	s_add_u32 s100, s18, s4
	s_addc_u32 s101, s19, s5
	s_add_i32 m0, s61, 0xc000
	ds_read_b128 v[182:185], v201
	ds_read_b128 v[210:213], v201 offset:2048
	ds_read_b128 v[186:189], v202
	ds_read_b128 v[214:217], v202 offset:2048
	ds_read_b128 v[218:221], v201 offset:4096
	ds_read_b128 v[226:229], v201 offset:6144
	ds_read_b128 v[222:225], v202 offset:4096
	ds_read_b128 v[230:233], v202 offset:6144
	global_load_lds_dwordx4 v170, s[100:101]
	s_add_i32 m0, s61, 0xe000
	s_nop 0
	global_load_lds_dwordx4 v168, s[100:101]
	s_waitcnt vmcnt(8)
	s_waitcnt lgkmcnt(0)
	s_barrier
	s_setprio 1
	s_waitcnt lgkmcnt(0)
	v_mfma_f32_16x16x128_f8f6f4 v[156:159], v[24:31], v[182:189], v[156:159]
	v_mfma_f32_16x16x128_f8f6f4 v[148:151], v[16:23], v[182:189], v[148:151]
	v_mfma_f32_16x16x128_f8f6f4 v[140:143], v[24:31], v[210:217], v[140:143]
	v_mfma_f32_16x16x128_f8f6f4 v[132:135], v[16:23], v[210:217], v[132:135]
	v_mfma_f32_16x16x128_f8f6f4 v[124:127], v[24:31], v[218:225], v[124:127]
	v_mfma_f32_16x16x128_f8f6f4 v[116:119], v[16:23], v[218:225], v[116:119]
	v_mfma_f32_16x16x128_f8f6f4 v[108:111], v[24:31], v[226:233], v[108:111]
	v_mfma_f32_16x16x128_f8f6f4 v[100:103], v[16:23], v[226:233], v[100:103]
	v_mfma_f32_16x16x128_f8f6f4 v[152:155], v[8:15], v[182:189], v[152:155]
	v_mfma_f32_16x16x128_f8f6f4 v[144:147], v[0:7], v[182:189], v[144:147]
	v_mfma_f32_16x16x128_f8f6f4 v[136:139], v[8:15], v[210:217], v[136:139]
	v_mfma_f32_16x16x128_f8f6f4 v[128:131], v[0:7], v[210:217], v[128:131]
	v_mfma_f32_16x16x128_f8f6f4 v[120:123], v[8:15], v[218:225], v[120:123]
	v_mfma_f32_16x16x128_f8f6f4 v[112:115], v[0:7], v[218:225], v[112:115]
	v_mfma_f32_16x16x128_f8f6f4 v[104:107], v[8:15], v[226:233], v[104:107]
	v_mfma_f32_16x16x128_f8f6f4 v[96:99], v[0:7], v[226:233], v[96:99]
	s_setprio 0
	s_barrier
	s_add_i32 s90, s72, s44
	s_mov_b32 m0, s90
	ds_read_b128 v[210:213], v201 offset:16384
	ds_read_b128 v[218:221], v201 offset:18432
	ds_read_b128 v[214:217], v202 offset:16384
	ds_read_b128 v[222:225], v202 offset:18432
	ds_read_b128 v[226:229], v201 offset:20480
	ds_read_b128 v[234:237], v201 offset:22528
	ds_read_b128 v[230:233], v202 offset:20480
	ds_read_b128 v[238:241], v202 offset:22528
	global_load_lds_dwordx4 v160, s[38:39]
	s_add_i32 m0, s90, 0x2000
	s_add_i32 s98, s74, s44
	global_load_lds_dwordx4 v162, s[38:39]
	s_mov_b32 m0, s98
	s_nop 0
	global_load_lds_dwordx4 v160, s[40:41]
	s_add_i32 m0, s98, 0x2000
	v_mov_b32_e32 v167, v165
	global_load_lds_dwordx4 v162, s[40:41]
	s_mov_b32 m0, s61
	s_nop 0
	global_load_lds_dwordx4 v164, s[36:37]
	s_mov_b32 m0, s62
	s_nop 0
	global_load_lds_dwordx4 v166, s[36:37]
	s_waitcnt vmcnt(8)
	s_waitcnt lgkmcnt(0)
	s_barrier
	s_setprio 1
	s_waitcnt lgkmcnt(0)
	v_mfma_f32_16x16x128_f8f6f4 v[92:95], v[24:31], v[210:217], v[92:95]
	v_mfma_f32_16x16x128_f8f6f4 v[84:87], v[16:23], v[210:217], v[84:87]
	v_mfma_f32_16x16x128_f8f6f4 v[76:79], v[24:31], v[218:225], v[76:79]
	v_mfma_f32_16x16x128_f8f6f4 v[68:71], v[16:23], v[218:225], v[68:71]
	v_mfma_f32_16x16x128_f8f6f4 v[60:63], v[24:31], v[226:233], v[60:63]
	v_mfma_f32_16x16x128_f8f6f4 v[52:55], v[16:23], v[226:233], v[52:55]
	v_mfma_f32_16x16x128_f8f6f4 v[44:47], v[24:31], v[234:241], v[44:47]
	v_mfma_f32_16x16x128_f8f6f4 v[36:39], v[16:23], v[234:241], v[36:39]
	v_mfma_f32_16x16x128_f8f6f4 v[88:91], v[8:15], v[210:217], v[88:91]
	v_mfma_f32_16x16x128_f8f6f4 v[80:83], v[0:7], v[210:217], v[80:83]
	v_mfma_f32_16x16x128_f8f6f4 v[72:75], v[8:15], v[218:225], v[72:75]
	v_mfma_f32_16x16x128_f8f6f4 v[64:67], v[0:7], v[218:225], v[64:67]
	v_mfma_f32_16x16x128_f8f6f4 v[56:59], v[8:15], v[226:233], v[56:59]
	v_mfma_f32_16x16x128_f8f6f4 v[48:51], v[0:7], v[226:233], v[48:51]
	v_mfma_f32_16x16x128_f8f6f4 v[40:43], v[8:15], v[234:241], v[40:43]
	v_mfma_f32_16x16x128_f8f6f4 v[32:35], v[0:7], v[234:241], v[32:35]
	s_setprio 0
	s_barrier
	ds_read_b128 v[0:3], v252 offset:32768
	ds_read_b128 v[4:7], v253 offset:32768
	ds_read_b128 v[8:11], v252 offset:34816
	ds_read_b128 v[12:15], v253 offset:34816
	ds_read_b128 v[16:19], v252 offset:49152
	ds_read_b128 v[20:23], v253 offset:49152
	ds_read_b128 v[24:27], v252 offset:51200
	ds_read_b128 v[28:31], v253 offset:51200
	s_mov_b32 m0, s63
	ds_read_b128 v[210:213], v201 offset:32768
	ds_read_b128 v[218:221], v201 offset:34816
	ds_read_b128 v[214:217], v202 offset:32768
	ds_read_b128 v[222:225], v202 offset:34816
	ds_read_b128 v[226:229], v201 offset:36864
	ds_read_b128 v[234:237], v201 offset:38912
	ds_read_b128 v[230:233], v202 offset:36864
	ds_read_b128 v[238:241], v202 offset:38912
	global_load_lds_dwordx4 v180, s[36:37]
	s_mov_b32 m0, s64
	s_nop 0
	global_load_lds_dwordx4 v178, s[36:37]
	s_waitcnt vmcnt(8)
	s_waitcnt lgkmcnt(0)
	s_barrier
	s_setprio 1
	s_waitcnt lgkmcnt(0)
	v_mfma_f32_16x16x128_f8f6f4 v[156:159], v[0:7], v[210:217], v[156:159]
	v_mfma_f32_16x16x128_f8f6f4 v[148:151], v[8:15], v[210:217], v[148:151]
	v_mfma_f32_16x16x128_f8f6f4 v[140:143], v[0:7], v[218:225], v[140:143]
	v_mfma_f32_16x16x128_f8f6f4 v[132:135], v[8:15], v[218:225], v[132:135]
	v_mfma_f32_16x16x128_f8f6f4 v[124:127], v[0:7], v[226:233], v[124:127]
	v_mfma_f32_16x16x128_f8f6f4 v[116:119], v[8:15], v[226:233], v[116:119]
	v_mfma_f32_16x16x128_f8f6f4 v[108:111], v[0:7], v[234:241], v[108:111]
	v_mfma_f32_16x16x128_f8f6f4 v[100:103], v[8:15], v[234:241], v[100:103]
	v_mfma_f32_16x16x128_f8f6f4 v[152:155], v[16:23], v[210:217], v[152:155]
	v_mfma_f32_16x16x128_f8f6f4 v[144:147], v[24:31], v[210:217], v[144:147]
	v_mfma_f32_16x16x128_f8f6f4 v[136:139], v[16:23], v[218:225], v[136:139]
	v_mfma_f32_16x16x128_f8f6f4 v[128:131], v[24:31], v[218:225], v[128:131]
	v_mfma_f32_16x16x128_f8f6f4 v[120:123], v[16:23], v[226:233], v[120:123]
	v_mfma_f32_16x16x128_f8f6f4 v[112:115], v[24:31], v[226:233], v[112:115]
	v_mfma_f32_16x16x128_f8f6f4 v[104:107], v[16:23], v[234:241], v[104:107]
	v_mfma_f32_16x16x128_f8f6f4 v[96:99], v[24:31], v[234:241], v[96:99]
	s_setprio 0
	s_barrier
	s_add_i32 s99, s44, 0x17f80
	s_mov_b32 m0, s99
	ds_read_b128 v[210:213], v201 offset:49152
	ds_read_b128 v[218:221], v201 offset:51200
	ds_read_b128 v[214:217], v202 offset:49152
	ds_read_b128 v[222:225], v202 offset:51200
	ds_read_b128 v[226:229], v201 offset:53248
	ds_read_b128 v[234:237], v201 offset:55296
	ds_read_b128 v[230:233], v202 offset:53248
	ds_read_b128 v[238:241], v202 offset:55296
	global_load_lds_dwordx4 v160, s[38:39] offset:128
	s_add_i32 m0, s99, 0x2000
	s_add_i32 s99, s44, 0x1bf80
	global_load_lds_dwordx4 v162, s[38:39] offset:128
	s_mov_b32 m0, s99
	s_nop 0
	global_load_lds_dwordx4 v160, s[40:41] offset:128
	s_add_i32 m0, s99, 0x2000
	s_nop 0
	global_load_lds_dwordx4 v162, s[40:41] offset:128
	s_add_i32 m0, s65, 0xffffff80
	s_nop 0
	global_load_lds_dwordx4 v164, s[36:37] offset:128
	s_add_i32 m0, s66, 0xffffff80
	s_nop 0
	global_load_lds_dwordx4 v166, s[36:37] offset:128
	s_waitcnt vmcnt(8)
	s_waitcnt lgkmcnt(0)
	s_barrier
	s_setprio 1
	s_waitcnt lgkmcnt(0)
	v_mfma_f32_16x16x128_f8f6f4 v[92:95], v[0:7], v[210:217], v[92:95]
	v_mfma_f32_16x16x128_f8f6f4 v[84:87], v[8:15], v[210:217], v[84:87]
	v_mfma_f32_16x16x128_f8f6f4 v[76:79], v[0:7], v[218:225], v[76:79]
	v_mfma_f32_16x16x128_f8f6f4 v[68:71], v[8:15], v[218:225], v[68:71]
	v_mfma_f32_16x16x128_f8f6f4 v[60:63], v[0:7], v[226:233], v[60:63]
	v_mfma_f32_16x16x128_f8f6f4 v[52:55], v[8:15], v[226:233], v[52:55]
	v_mfma_f32_16x16x128_f8f6f4 v[44:47], v[0:7], v[234:241], v[44:47]
	v_mfma_f32_16x16x128_f8f6f4 v[36:39], v[8:15], v[234:241], v[36:39]
	v_mfma_f32_16x16x128_f8f6f4 v[88:91], v[16:23], v[210:217], v[88:91]
	v_mfma_f32_16x16x128_f8f6f4 v[80:83], v[24:31], v[210:217], v[80:83]
	v_mfma_f32_16x16x128_f8f6f4 v[72:75], v[16:23], v[218:225], v[72:75]
	v_mfma_f32_16x16x128_f8f6f4 v[64:67], v[24:31], v[218:225], v[64:67]
	v_mfma_f32_16x16x128_f8f6f4 v[56:59], v[16:23], v[226:233], v[56:59]
	v_mfma_f32_16x16x128_f8f6f4 v[48:51], v[24:31], v[226:233], v[48:51]
	v_mfma_f32_16x16x128_f8f6f4 v[40:43], v[16:23], v[234:241], v[40:43]
	v_mfma_f32_16x16x128_f8f6f4 v[32:35], v[24:31], v[234:241], v[32:35]
	s_setprio 0
	s_barrier
	s_add_i32 s89, s89, 2
	s_add_u32 s4, s4, 0x100
	s_addc_u32 s5, s5, 0
	s_cmp_gt_u32 s89, 5
	s_cbranch_scc1 .LBB0_593

.LBB0_672:
	s_add_u32 s36, s6, s34
	s_addc_u32 s37, s7, s35
	s_add_u32 s38, s36, 0x12c00100
	s_addc_u32 s39, s37, 0
	ds_read_b128 v[24:27], v252
	ds_read_b128 v[28:31], v253
	s_and_b64 s[36:37], s[40:41], exec
	ds_read_b128 v[16:19], v252 offset:2048
	ds_read_b128 v[20:23], v253 offset:2048
	s_cselect_b32 s37, s9, s39
	s_cselect_b32 s36, s8, s38
	s_add_u32 s86, s27, s34
	ds_read_b128 v[8:11], v252 offset:16384
	ds_read_b128 v[12:15], v253 offset:16384
	s_addc_u32 s87, s82, s35
	ds_read_b128 v[0:3], v252 offset:18432
	ds_read_b128 v[4:7], v253 offset:18432
	s_and_b64 s[38:39], s[40:41], exec
	s_cselect_b32 s39, s29, s87
	s_cselect_b32 s38, s28, s86
	s_add_u32 s86, s83, s34
	s_addc_u32 s87, s84, s35
	s_and_b64 s[40:41], s[40:41], exec
	s_cselect_b32 s41, s31, s87
	s_cselect_b32 s40, s30, s86
	s_add_u32 s100, s16, s34
	s_addc_u32 s101, s17, s35
	s_add_i32 m0, s59, 0xc000
	ds_read_b128 v[186:189], v207
	ds_read_b128 v[216:219], v207 offset:2048
	ds_read_b128 v[190:193], v208
	ds_read_b128 v[220:223], v208 offset:2048
	ds_read_b128 v[224:227], v207 offset:4096
	ds_read_b128 v[232:235], v207 offset:6144
	ds_read_b128 v[228:231], v208 offset:4096
	ds_read_b128 v[236:239], v208 offset:6144
	global_load_lds_dwordx4 v166, s[100:101]
	s_add_i32 m0, s59, 0xe000
	s_nop 0
	global_load_lds_dwordx4 v168, s[100:101]
	s_waitcnt vmcnt(8)
	s_waitcnt lgkmcnt(0)
	s_barrier
	s_setprio 1
	s_waitcnt lgkmcnt(0)
	v_mfma_f32_16x16x128_f8f6f4 v[156:159], v[24:31], v[186:193], v[156:159]
	v_mfma_f32_16x16x128_f8f6f4 v[152:155], v[16:23], v[186:193], v[152:155]
	v_mfma_f32_16x16x128_f8f6f4 v[140:143], v[24:31], v[216:223], v[140:143]
	v_mfma_f32_16x16x128_f8f6f4 v[136:139], v[16:23], v[216:223], v[136:139]
	v_mfma_f32_16x16x128_f8f6f4 v[124:127], v[24:31], v[224:231], v[124:127]
	v_mfma_f32_16x16x128_f8f6f4 v[120:123], v[16:23], v[224:231], v[120:123]
	v_mfma_f32_16x16x128_f8f6f4 v[108:111], v[24:31], v[232:239], v[108:111]
	v_mfma_f32_16x16x128_f8f6f4 v[104:107], v[16:23], v[232:239], v[104:107]
	v_mfma_f32_16x16x128_f8f6f4 v[148:151], v[8:15], v[186:193], v[148:151]
	v_mfma_f32_16x16x128_f8f6f4 v[144:147], v[0:7], v[186:193], v[144:147]
	v_mfma_f32_16x16x128_f8f6f4 v[132:135], v[8:15], v[216:223], v[132:135]
	v_mfma_f32_16x16x128_f8f6f4 v[128:131], v[0:7], v[216:223], v[128:131]
	v_mfma_f32_16x16x128_f8f6f4 v[116:119], v[8:15], v[224:231], v[116:119]
	v_mfma_f32_16x16x128_f8f6f4 v[112:115], v[0:7], v[224:231], v[112:115]
	v_mfma_f32_16x16x128_f8f6f4 v[100:103], v[8:15], v[232:239], v[100:103]
	v_mfma_f32_16x16x128_f8f6f4 v[96:99], v[0:7], v[232:239], v[96:99]
	s_setprio 0
	s_barrier
	s_add_i32 s86, s69, s42
	s_mov_b32 m0, s86
	ds_read_b128 v[216:219], v207 offset:16384
	ds_read_b128 v[224:227], v207 offset:18432
	ds_read_b128 v[220:223], v208 offset:16384
	ds_read_b128 v[228:231], v208 offset:18432
	ds_read_b128 v[232:235], v207 offset:20480
	ds_read_b128 v[240:243], v207 offset:22528
	ds_read_b128 v[236:239], v208 offset:20480
	ds_read_b128 v[244:247], v208 offset:22528
	global_load_lds_dwordx4 v160, s[38:39]
	s_add_i32 m0, s86, 0x2000
	s_add_i32 s98, s71, s42
	global_load_lds_dwordx4 v162, s[38:39]
	s_mov_b32 m0, s98
	s_nop 0
	global_load_lds_dwordx4 v160, s[40:41]
	s_add_i32 m0, s98, 0x2000
	v_mov_b32_e32 v173, v165
	global_load_lds_dwordx4 v162, s[40:41]
	s_mov_b32 m0, s59
	s_nop 0
	global_load_lds_dwordx4 v164, s[36:37]
	s_mov_b32 m0, s60
	s_nop 0
	global_load_lds_dwordx4 v172, s[36:37]
	s_waitcnt vmcnt(8)
	s_waitcnt lgkmcnt(0)
	s_barrier
	s_setprio 1
	s_waitcnt lgkmcnt(0)
	v_mfma_f32_16x16x128_f8f6f4 v[92:95], v[24:31], v[216:223], v[92:95]
	v_mfma_f32_16x16x128_f8f6f4 v[88:91], v[16:23], v[216:223], v[88:91]
	v_mfma_f32_16x16x128_f8f6f4 v[76:79], v[24:31], v[224:231], v[76:79]
	v_mfma_f32_16x16x128_f8f6f4 v[72:75], v[16:23], v[224:231], v[72:75]
	v_mfma_f32_16x16x128_f8f6f4 v[60:63], v[24:31], v[232:239], v[60:63]
	v_mfma_f32_16x16x128_f8f6f4 v[56:59], v[16:23], v[232:239], v[56:59]
	v_mfma_f32_16x16x128_f8f6f4 v[44:47], v[24:31], v[240:247], v[44:47]
	v_mfma_f32_16x16x128_f8f6f4 v[40:43], v[16:23], v[240:247], v[40:43]
	v_mfma_f32_16x16x128_f8f6f4 v[84:87], v[8:15], v[216:223], v[84:87]
	v_mfma_f32_16x16x128_f8f6f4 v[80:83], v[0:7], v[216:223], v[80:83]
	v_mfma_f32_16x16x128_f8f6f4 v[68:71], v[8:15], v[224:231], v[68:71]
	v_mfma_f32_16x16x128_f8f6f4 v[64:67], v[0:7], v[224:231], v[64:67]
	v_mfma_f32_16x16x128_f8f6f4 v[52:55], v[8:15], v[232:239], v[52:55]
	v_mfma_f32_16x16x128_f8f6f4 v[48:51], v[0:7], v[232:239], v[48:51]
	v_mfma_f32_16x16x128_f8f6f4 v[36:39], v[8:15], v[240:247], v[36:39]
	v_mfma_f32_16x16x128_f8f6f4 v[32:35], v[0:7], v[240:247], v[32:35]
	s_setprio 0
	s_barrier
	ds_read_b128 v[0:3], v252 offset:32768
	ds_read_b128 v[4:7], v253 offset:32768
	ds_read_b128 v[8:11], v252 offset:34816
	ds_read_b128 v[12:15], v253 offset:34816
	ds_read_b128 v[16:19], v252 offset:49152
	ds_read_b128 v[20:23], v253 offset:49152
	ds_read_b128 v[24:27], v252 offset:51200
	ds_read_b128 v[28:31], v253 offset:51200
	s_mov_b32 m0, s61
	ds_read_b128 v[216:219], v207 offset:32768
	ds_read_b128 v[224:227], v207 offset:34816
	ds_read_b128 v[220:223], v208 offset:32768
	ds_read_b128 v[228:231], v208 offset:34816
	ds_read_b128 v[232:235], v207 offset:36864
	ds_read_b128 v[240:243], v207 offset:38912
	ds_read_b128 v[236:239], v208 offset:36864
	ds_read_b128 v[244:247], v208 offset:38912
	global_load_lds_dwordx4 v184, s[36:37]
	s_mov_b32 m0, s62
	s_nop 0
	global_load_lds_dwordx4 v182, s[36:37]
	s_waitcnt vmcnt(8)
	s_waitcnt lgkmcnt(0)
	s_barrier
	s_setprio 1
	s_waitcnt lgkmcnt(0)
	v_mfma_f32_16x16x128_f8f6f4 v[156:159], v[0:7], v[216:223], v[156:159]
	v_mfma_f32_16x16x128_f8f6f4 v[152:155], v[8:15], v[216:223], v[152:155]
	v_mfma_f32_16x16x128_f8f6f4 v[140:143], v[0:7], v[224:231], v[140:143]
	v_mfma_f32_16x16x128_f8f6f4 v[136:139], v[8:15], v[224:231], v[136:139]
	v_mfma_f32_16x16x128_f8f6f4 v[124:127], v[0:7], v[232:239], v[124:127]
	v_mfma_f32_16x16x128_f8f6f4 v[120:123], v[8:15], v[232:239], v[120:123]
	v_mfma_f32_16x16x128_f8f6f4 v[108:111], v[0:7], v[240:247], v[108:111]
	v_mfma_f32_16x16x128_f8f6f4 v[104:107], v[8:15], v[240:247], v[104:107]
	v_mfma_f32_16x16x128_f8f6f4 v[148:151], v[16:23], v[216:223], v[148:151]
	v_mfma_f32_16x16x128_f8f6f4 v[144:147], v[24:31], v[216:223], v[144:147]
	v_mfma_f32_16x16x128_f8f6f4 v[132:135], v[16:23], v[224:231], v[132:135]
	v_mfma_f32_16x16x128_f8f6f4 v[128:131], v[24:31], v[224:231], v[128:131]
	v_mfma_f32_16x16x128_f8f6f4 v[116:119], v[16:23], v[232:239], v[116:119]
	v_mfma_f32_16x16x128_f8f6f4 v[112:115], v[24:31], v[232:239], v[112:115]
	v_mfma_f32_16x16x128_f8f6f4 v[100:103], v[16:23], v[240:247], v[100:103]
	v_mfma_f32_16x16x128_f8f6f4 v[96:99], v[24:31], v[240:247], v[96:99]
	s_setprio 0
	s_barrier
	s_add_i32 s99, s42, 0x17f80
	s_mov_b32 m0, s99
	ds_read_b128 v[216:219], v207 offset:49152
	ds_read_b128 v[224:227], v207 offset:51200
	ds_read_b128 v[220:223], v208 offset:49152
	ds_read_b128 v[228:231], v208 offset:51200
	ds_read_b128 v[232:235], v207 offset:53248
	ds_read_b128 v[240:243], v207 offset:55296
	ds_read_b128 v[236:239], v208 offset:53248
	ds_read_b128 v[244:247], v208 offset:55296
	global_load_lds_dwordx4 v160, s[38:39] offset:128
	s_add_i32 m0, s99, 0x2000
	s_add_i32 s99, s42, 0x1bf80
	global_load_lds_dwordx4 v162, s[38:39] offset:128
	s_mov_b32 m0, s99
	s_nop 0
	global_load_lds_dwordx4 v160, s[40:41] offset:128
	s_add_i32 m0, s99, 0x2000
	s_nop 0
	global_load_lds_dwordx4 v162, s[40:41] offset:128
	s_add_i32 m0, s63, 0xffffff80
	s_nop 0
	global_load_lds_dwordx4 v164, s[36:37] offset:128
	s_add_i32 m0, s64, 0xffffff80
	s_nop 0
	global_load_lds_dwordx4 v172, s[36:37] offset:128
	s_waitcnt vmcnt(8)
	s_waitcnt lgkmcnt(0)
	s_barrier
	s_setprio 1
	s_waitcnt lgkmcnt(0)
	v_mfma_f32_16x16x128_f8f6f4 v[92:95], v[0:7], v[216:223], v[92:95]
	v_mfma_f32_16x16x128_f8f6f4 v[88:91], v[8:15], v[216:223], v[88:91]
	v_mfma_f32_16x16x128_f8f6f4 v[76:79], v[0:7], v[224:231], v[76:79]
	v_mfma_f32_16x16x128_f8f6f4 v[72:75], v[8:15], v[224:231], v[72:75]
	v_mfma_f32_16x16x128_f8f6f4 v[60:63], v[0:7], v[232:239], v[60:63]
	v_mfma_f32_16x16x128_f8f6f4 v[56:59], v[8:15], v[232:239], v[56:59]
	v_mfma_f32_16x16x128_f8f6f4 v[44:47], v[0:7], v[240:247], v[44:47]
	v_mfma_f32_16x16x128_f8f6f4 v[40:43], v[8:15], v[240:247], v[40:43]
	v_mfma_f32_16x16x128_f8f6f4 v[84:87], v[16:23], v[216:223], v[84:87]
	v_mfma_f32_16x16x128_f8f6f4 v[80:83], v[24:31], v[216:223], v[80:83]
	v_mfma_f32_16x16x128_f8f6f4 v[68:71], v[16:23], v[224:231], v[68:71]
	v_mfma_f32_16x16x128_f8f6f4 v[64:67], v[24:31], v[224:231], v[64:67]
	v_mfma_f32_16x16x128_f8f6f4 v[52:55], v[16:23], v[232:239], v[52:55]
	v_mfma_f32_16x16x128_f8f6f4 v[48:51], v[24:31], v[232:239], v[48:51]
	v_mfma_f32_16x16x128_f8f6f4 v[36:39], v[16:23], v[240:247], v[36:39]
	v_mfma_f32_16x16x128_f8f6f4 v[32:35], v[24:31], v[240:247], v[32:35]
	s_setprio 0
	s_barrier
	s_add_i32 s85, s85, 2
	s_add_u32 s34, s34, 0x100
	s_addc_u32 s35, s35, 0
	s_cmp_gt_u32 s85, 5
	s_cbranch_scc1 .LBB0_675

.LBB0_817:
	s_add_u32 s28, s10, s26
	s_addc_u32 s29, s11, s27
	s_add_u32 s30, s28, 0x38000100
	s_addc_u32 s31, s29, 0
	ds_read_b128 v[24:27], v252
	ds_read_b128 v[28:31], v253
	s_and_b64 s[28:29], s[34:35], exec
	ds_read_b128 v[16:19], v252 offset:2048
	ds_read_b128 v[20:23], v253 offset:2048
	s_cselect_b32 s29, s1, s31
	s_cselect_b32 s28, s0, s30
	s_add_u32 s61, s56, s26
	ds_read_b128 v[8:11], v252 offset:16384
	ds_read_b128 v[12:15], v253 offset:16384
	s_addc_u32 s62, s57, s27
	ds_read_b128 v[0:3], v252 offset:18432
	ds_read_b128 v[4:7], v253 offset:18432
	s_and_b64 s[30:31], s[34:35], exec
	s_cselect_b32 s31, s23, s62
	s_cselect_b32 s30, s22, s61
	s_add_u32 s61, s58, s26
	s_addc_u32 s62, s59, s27
	s_and_b64 s[34:35], s[34:35], exec
	s_cselect_b32 s35, s25, s62
	s_cselect_b32 s34, s24, s61
	s_add_u32 s100, s14, s26
	s_addc_u32 s101, s15, s27
	s_add_i32 m0, s37, 0xc000
	ds_read_b128 v[186:189], v207
	ds_read_b128 v[216:219], v207 offset:2048
	ds_read_b128 v[190:193], v208
	ds_read_b128 v[220:223], v208 offset:2048
	ds_read_b128 v[224:227], v207 offset:4096
	ds_read_b128 v[232:235], v207 offset:6144
	ds_read_b128 v[228:231], v208 offset:4096
	ds_read_b128 v[236:239], v208 offset:6144
	global_load_lds_dwordx4 v168, s[100:101]
	s_add_i32 m0, s37, 0xe000
	s_nop 0
	global_load_lds_dwordx4 v170, s[100:101]
	s_waitcnt vmcnt(8)
	s_waitcnt lgkmcnt(0)
	s_barrier
	s_setprio 1
	s_waitcnt lgkmcnt(0)
	v_mfma_f32_16x16x128_f8f6f4 v[156:159], v[24:31], v[186:193], v[156:159]
	v_mfma_f32_16x16x128_f8f6f4 v[152:155], v[16:23], v[186:193], v[152:155]
	v_mfma_f32_16x16x128_f8f6f4 v[140:143], v[24:31], v[216:223], v[140:143]
	v_mfma_f32_16x16x128_f8f6f4 v[136:139], v[16:23], v[216:223], v[136:139]
	v_mfma_f32_16x16x128_f8f6f4 v[124:127], v[24:31], v[224:231], v[124:127]
	v_mfma_f32_16x16x128_f8f6f4 v[120:123], v[16:23], v[224:231], v[120:123]
	v_mfma_f32_16x16x128_f8f6f4 v[108:111], v[24:31], v[232:239], v[108:111]
	v_mfma_f32_16x16x128_f8f6f4 v[104:107], v[16:23], v[232:239], v[104:107]
	v_mfma_f32_16x16x128_f8f6f4 v[148:151], v[8:15], v[186:193], v[148:151]
	v_mfma_f32_16x16x128_f8f6f4 v[144:147], v[0:7], v[186:193], v[144:147]
	v_mfma_f32_16x16x128_f8f6f4 v[132:135], v[8:15], v[216:223], v[132:135]
	v_mfma_f32_16x16x128_f8f6f4 v[128:131], v[0:7], v[216:223], v[128:131]
	v_mfma_f32_16x16x128_f8f6f4 v[116:119], v[8:15], v[224:231], v[116:119]
	v_mfma_f32_16x16x128_f8f6f4 v[112:115], v[0:7], v[224:231], v[112:115]
	v_mfma_f32_16x16x128_f8f6f4 v[100:103], v[8:15], v[232:239], v[100:103]
	v_mfma_f32_16x16x128_f8f6f4 v[96:99], v[0:7], v[232:239], v[96:99]
	s_setprio 0
	s_barrier
	s_add_i32 s61, s44, s36
	s_mov_b32 m0, s61
	ds_read_b128 v[216:219], v207 offset:16384
	ds_read_b128 v[224:227], v207 offset:18432
	ds_read_b128 v[220:223], v208 offset:16384
	ds_read_b128 v[228:231], v208 offset:18432
	ds_read_b128 v[232:235], v207 offset:20480
	ds_read_b128 v[240:243], v207 offset:22528
	ds_read_b128 v[236:239], v208 offset:20480
	ds_read_b128 v[244:247], v208 offset:22528
	global_load_lds_dwordx4 v160, s[30:31]
	s_add_i32 m0, s61, 0x2000
	s_add_i32 s98, s46, s36
	global_load_lds_dwordx4 v162, s[30:31]
	s_mov_b32 m0, s98
	s_nop 0
	global_load_lds_dwordx4 v160, s[34:35]
	s_add_i32 m0, s98, 0x2000
	v_mov_b32_e32 v167, v165
	global_load_lds_dwordx4 v162, s[34:35]
	s_mov_b32 m0, s37
	s_nop 0
	global_load_lds_dwordx4 v164, s[28:29]
	s_mov_b32 m0, s38
	s_nop 0
	global_load_lds_dwordx4 v166, s[28:29]
	s_waitcnt vmcnt(8)
	s_waitcnt lgkmcnt(0)
	s_barrier
	s_setprio 1
	s_waitcnt lgkmcnt(0)
	v_mfma_f32_16x16x128_f8f6f4 v[92:95], v[24:31], v[216:223], v[92:95]
	v_mfma_f32_16x16x128_f8f6f4 v[88:91], v[16:23], v[216:223], v[88:91]
	v_mfma_f32_16x16x128_f8f6f4 v[76:79], v[24:31], v[224:231], v[76:79]
	v_mfma_f32_16x16x128_f8f6f4 v[72:75], v[16:23], v[224:231], v[72:75]
	v_mfma_f32_16x16x128_f8f6f4 v[60:63], v[24:31], v[232:239], v[60:63]
	v_mfma_f32_16x16x128_f8f6f4 v[56:59], v[16:23], v[232:239], v[56:59]
	v_mfma_f32_16x16x128_f8f6f4 v[44:47], v[24:31], v[240:247], v[44:47]
	v_mfma_f32_16x16x128_f8f6f4 v[40:43], v[16:23], v[240:247], v[40:43]
	v_mfma_f32_16x16x128_f8f6f4 v[84:87], v[8:15], v[216:223], v[84:87]
	v_mfma_f32_16x16x128_f8f6f4 v[80:83], v[0:7], v[216:223], v[80:83]
	v_mfma_f32_16x16x128_f8f6f4 v[68:71], v[8:15], v[224:231], v[68:71]
	v_mfma_f32_16x16x128_f8f6f4 v[64:67], v[0:7], v[224:231], v[64:67]
	v_mfma_f32_16x16x128_f8f6f4 v[52:55], v[8:15], v[232:239], v[52:55]
	v_mfma_f32_16x16x128_f8f6f4 v[48:51], v[0:7], v[232:239], v[48:51]
	v_mfma_f32_16x16x128_f8f6f4 v[36:39], v[8:15], v[240:247], v[36:39]
	v_mfma_f32_16x16x128_f8f6f4 v[32:35], v[0:7], v[240:247], v[32:35]
	s_setprio 0
	s_barrier
	ds_read_b128 v[0:3], v252 offset:32768
	ds_read_b128 v[4:7], v253 offset:32768
	ds_read_b128 v[8:11], v252 offset:34816
	ds_read_b128 v[12:15], v253 offset:34816
	ds_read_b128 v[16:19], v252 offset:49152
	ds_read_b128 v[20:23], v253 offset:49152
	ds_read_b128 v[24:27], v252 offset:51200
	ds_read_b128 v[28:31], v253 offset:51200
	s_mov_b32 m0, s39
	ds_read_b128 v[216:219], v207 offset:32768
	ds_read_b128 v[224:227], v207 offset:34816
	ds_read_b128 v[220:223], v208 offset:32768
	ds_read_b128 v[228:231], v208 offset:34816
	ds_read_b128 v[232:235], v207 offset:36864
	ds_read_b128 v[240:243], v207 offset:38912
	ds_read_b128 v[236:239], v208 offset:36864
	ds_read_b128 v[244:247], v208 offset:38912
	global_load_lds_dwordx4 v184, s[28:29]
	s_mov_b32 m0, s40
	s_nop 0
	global_load_lds_dwordx4 v182, s[28:29]
	s_waitcnt vmcnt(8)
	s_waitcnt lgkmcnt(0)
	s_barrier
	s_setprio 1
	s_waitcnt lgkmcnt(0)
	v_mfma_f32_16x16x128_f8f6f4 v[156:159], v[0:7], v[216:223], v[156:159]
	v_mfma_f32_16x16x128_f8f6f4 v[152:155], v[8:15], v[216:223], v[152:155]
	v_mfma_f32_16x16x128_f8f6f4 v[140:143], v[0:7], v[224:231], v[140:143]
	v_mfma_f32_16x16x128_f8f6f4 v[136:139], v[8:15], v[224:231], v[136:139]
	v_mfma_f32_16x16x128_f8f6f4 v[124:127], v[0:7], v[232:239], v[124:127]
	v_mfma_f32_16x16x128_f8f6f4 v[120:123], v[8:15], v[232:239], v[120:123]
	v_mfma_f32_16x16x128_f8f6f4 v[108:111], v[0:7], v[240:247], v[108:111]
	v_mfma_f32_16x16x128_f8f6f4 v[104:107], v[8:15], v[240:247], v[104:107]
	v_mfma_f32_16x16x128_f8f6f4 v[148:151], v[16:23], v[216:223], v[148:151]
	v_mfma_f32_16x16x128_f8f6f4 v[144:147], v[24:31], v[216:223], v[144:147]
	v_mfma_f32_16x16x128_f8f6f4 v[132:135], v[16:23], v[224:231], v[132:135]
	v_mfma_f32_16x16x128_f8f6f4 v[128:131], v[24:31], v[224:231], v[128:131]
	v_mfma_f32_16x16x128_f8f6f4 v[116:119], v[16:23], v[232:239], v[116:119]
	v_mfma_f32_16x16x128_f8f6f4 v[112:115], v[24:31], v[232:239], v[112:115]
	v_mfma_f32_16x16x128_f8f6f4 v[100:103], v[16:23], v[240:247], v[100:103]
	v_mfma_f32_16x16x128_f8f6f4 v[96:99], v[24:31], v[240:247], v[96:99]
	s_setprio 0
	s_barrier
	s_add_i32 s99, s36, 0x17f80
	s_mov_b32 m0, s99
	ds_read_b128 v[216:219], v207 offset:49152
	ds_read_b128 v[224:227], v207 offset:51200
	ds_read_b128 v[220:223], v208 offset:49152
	ds_read_b128 v[228:231], v208 offset:51200
	ds_read_b128 v[232:235], v207 offset:53248
	ds_read_b128 v[240:243], v207 offset:55296
	ds_read_b128 v[236:239], v208 offset:53248
	ds_read_b128 v[244:247], v208 offset:55296
	global_load_lds_dwordx4 v160, s[30:31] offset:128
	s_add_i32 m0, s99, 0x2000
	s_add_i32 s99, s36, 0x1bf80
	global_load_lds_dwordx4 v162, s[30:31] offset:128
	s_mov_b32 m0, s99
	s_nop 0
	global_load_lds_dwordx4 v160, s[34:35] offset:128
	s_add_i32 m0, s99, 0x2000
	s_nop 0
	global_load_lds_dwordx4 v162, s[34:35] offset:128
	s_add_i32 m0, s41, 0xffffff80
	s_nop 0
	global_load_lds_dwordx4 v164, s[28:29] offset:128
	s_add_i32 m0, s42, 0xffffff80
	s_nop 0
	global_load_lds_dwordx4 v166, s[28:29] offset:128
	s_waitcnt vmcnt(8)
	s_waitcnt lgkmcnt(0)
	s_barrier
	s_setprio 1
	s_waitcnt lgkmcnt(0)
	v_mfma_f32_16x16x128_f8f6f4 v[92:95], v[0:7], v[216:223], v[92:95]
	v_mfma_f32_16x16x128_f8f6f4 v[88:91], v[8:15], v[216:223], v[88:91]
	v_mfma_f32_16x16x128_f8f6f4 v[76:79], v[0:7], v[224:231], v[76:79]
	v_mfma_f32_16x16x128_f8f6f4 v[72:75], v[8:15], v[224:231], v[72:75]
	v_mfma_f32_16x16x128_f8f6f4 v[60:63], v[0:7], v[232:239], v[60:63]
	v_mfma_f32_16x16x128_f8f6f4 v[56:59], v[8:15], v[232:239], v[56:59]
	v_mfma_f32_16x16x128_f8f6f4 v[44:47], v[0:7], v[240:247], v[44:47]
	v_mfma_f32_16x16x128_f8f6f4 v[40:43], v[8:15], v[240:247], v[40:43]
	v_mfma_f32_16x16x128_f8f6f4 v[84:87], v[16:23], v[216:223], v[84:87]
	v_mfma_f32_16x16x128_f8f6f4 v[80:83], v[24:31], v[216:223], v[80:83]
	v_mfma_f32_16x16x128_f8f6f4 v[68:71], v[16:23], v[224:231], v[68:71]
	v_mfma_f32_16x16x128_f8f6f4 v[64:67], v[24:31], v[224:231], v[64:67]
	v_mfma_f32_16x16x128_f8f6f4 v[52:55], v[16:23], v[232:239], v[52:55]
	v_mfma_f32_16x16x128_f8f6f4 v[48:51], v[24:31], v[232:239], v[48:51]
	v_mfma_f32_16x16x128_f8f6f4 v[36:39], v[16:23], v[240:247], v[36:39]
	v_mfma_f32_16x16x128_f8f6f4 v[32:35], v[24:31], v[240:247], v[32:35]
	s_setprio 0
	s_barrier
	s_add_i32 s60, s60, 2
	s_add_u32 s26, s26, 0x100
	s_addc_u32 s27, s27, 0
	s_cmp_gt_u32 s60, 5
	s_cbranch_scc1 .LBB0_820

.LBB0_1549:
	s_add_u32 s26, s4, s24
	s_addc_u32 s27, s5, s25
	s_add_u32 s28, s26, 0x28000100
	s_addc_u32 s29, s27, 0
	ds_read_b128 v[24:27], v252
	ds_read_b128 v[28:31], v253
	s_and_b64 s[26:27], s[30:31], exec
	ds_read_b128 v[16:19], v252 offset:2048
	ds_read_b128 v[20:23], v253 offset:2048
	s_cselect_b32 s27, s7, s29
	s_cselect_b32 s26, s6, s28
	s_add_u32 s63, s58, s24
	ds_read_b128 v[8:11], v252 offset:16384
	ds_read_b128 v[12:15], v253 offset:16384
	s_addc_u32 s64, s59, s25
	ds_read_b128 v[0:3], v252 offset:18432
	ds_read_b128 v[4:7], v253 offset:18432
	s_and_b64 s[28:29], s[30:31], exec
	s_cselect_b32 s29, s21, s64
	s_cselect_b32 s28, s20, s63
	s_add_u32 s63, s60, s24
	s_addc_u32 s64, s61, s25
	s_and_b64 s[30:31], s[30:31], exec
	s_cselect_b32 s31, s23, s64
	s_cselect_b32 s30, s22, s63
	s_add_u32 s100, s14, s24
	s_addc_u32 s101, s15, s25
	s_add_i32 m0, s35, 0xc000
	ds_read_b128 v[186:189], v206
	ds_read_b128 v[214:217], v206 offset:2048
	ds_read_b128 v[190:193], v207
	ds_read_b128 v[218:221], v207 offset:2048
	ds_read_b128 v[222:225], v206 offset:4096
	ds_read_b128 v[230:233], v206 offset:6144
	ds_read_b128 v[226:229], v207 offset:4096
	ds_read_b128 v[234:237], v207 offset:6144
	global_load_lds_dwordx4 v168, s[100:101]
	s_add_i32 m0, s35, 0xe000
	s_nop 0
	global_load_lds_dwordx4 v170, s[100:101]
	s_waitcnt vmcnt(8)
	s_waitcnt lgkmcnt(0)
	s_barrier
	s_setprio 1
	s_waitcnt lgkmcnt(0)
	v_mfma_f32_16x16x128_f8f6f4 v[156:159], v[24:31], v[186:193], v[156:159]
	v_mfma_f32_16x16x128_f8f6f4 v[152:155], v[16:23], v[186:193], v[152:155]
	v_mfma_f32_16x16x128_f8f6f4 v[144:147], v[24:31], v[214:221], v[144:147]
	v_mfma_f32_16x16x128_f8f6f4 v[136:139], v[16:23], v[214:221], v[136:139]
	v_mfma_f32_16x16x128_f8f6f4 v[124:127], v[24:31], v[222:229], v[124:127]
	v_mfma_f32_16x16x128_f8f6f4 v[120:123], v[16:23], v[222:229], v[120:123]
	v_mfma_f32_16x16x128_f8f6f4 v[112:115], v[24:31], v[230:237], v[112:115]
	v_mfma_f32_16x16x128_f8f6f4 v[104:107], v[16:23], v[230:237], v[104:107]
	v_mfma_f32_16x16x128_f8f6f4 v[148:151], v[8:15], v[186:193], v[148:151]
	v_mfma_f32_16x16x128_f8f6f4 v[140:143], v[0:7], v[186:193], v[140:143]
	v_mfma_f32_16x16x128_f8f6f4 v[132:135], v[8:15], v[214:221], v[132:135]
	v_mfma_f32_16x16x128_f8f6f4 v[128:131], v[0:7], v[214:221], v[128:131]
	v_mfma_f32_16x16x128_f8f6f4 v[116:119], v[8:15], v[222:229], v[116:119]
	v_mfma_f32_16x16x128_f8f6f4 v[108:111], v[0:7], v[222:229], v[108:111]
	v_mfma_f32_16x16x128_f8f6f4 v[100:103], v[8:15], v[230:237], v[100:103]
	v_mfma_f32_16x16x128_f8f6f4 v[96:99], v[0:7], v[230:237], v[96:99]
	s_setprio 0
	s_barrier
	s_add_i32 s63, s46, s34
	s_mov_b32 m0, s63
	ds_read_b128 v[214:217], v206 offset:16384
	ds_read_b128 v[222:225], v206 offset:18432
	ds_read_b128 v[218:221], v207 offset:16384
	ds_read_b128 v[226:229], v207 offset:18432
	ds_read_b128 v[230:233], v206 offset:20480
	ds_read_b128 v[238:241], v206 offset:22528
	ds_read_b128 v[234:237], v207 offset:20480
	ds_read_b128 v[242:245], v207 offset:22528
	global_load_lds_dwordx4 v160, s[28:29]
	s_add_i32 m0, s63, 0x2000
	s_add_i32 s98, s48, s34
	global_load_lds_dwordx4 v162, s[28:29]
	s_mov_b32 m0, s98
	s_nop 0
	global_load_lds_dwordx4 v160, s[30:31]
	s_add_i32 m0, s98, 0x2000
	v_mov_b32_e32 v167, v165
	global_load_lds_dwordx4 v162, s[30:31]
	s_mov_b32 m0, s35
	s_nop 0
	global_load_lds_dwordx4 v164, s[26:27]
	s_mov_b32 m0, s36
	s_nop 0
	global_load_lds_dwordx4 v166, s[26:27]
	s_waitcnt vmcnt(8)
	s_waitcnt lgkmcnt(0)
	s_barrier
	s_setprio 1
	s_waitcnt lgkmcnt(0)
	v_mfma_f32_16x16x128_f8f6f4 v[92:95], v[24:31], v[214:221], v[92:95]
	v_mfma_f32_16x16x128_f8f6f4 v[88:91], v[16:23], v[214:221], v[88:91]
	v_mfma_f32_16x16x128_f8f6f4 v[80:83], v[24:31], v[222:229], v[80:83]
	v_mfma_f32_16x16x128_f8f6f4 v[72:75], v[16:23], v[222:229], v[72:75]
	v_mfma_f32_16x16x128_f8f6f4 v[60:63], v[24:31], v[230:237], v[60:63]
	v_mfma_f32_16x16x128_f8f6f4 v[56:59], v[16:23], v[230:237], v[56:59]
	v_mfma_f32_16x16x128_f8f6f4 v[48:51], v[24:31], v[238:245], v[48:51]
	v_mfma_f32_16x16x128_f8f6f4 v[40:43], v[16:23], v[238:245], v[40:43]
	v_mfma_f32_16x16x128_f8f6f4 v[84:87], v[8:15], v[214:221], v[84:87]
	v_mfma_f32_16x16x128_f8f6f4 v[76:79], v[0:7], v[214:221], v[76:79]
	v_mfma_f32_16x16x128_f8f6f4 v[68:71], v[8:15], v[222:229], v[68:71]
	v_mfma_f32_16x16x128_f8f6f4 v[64:67], v[0:7], v[222:229], v[64:67]
	v_mfma_f32_16x16x128_f8f6f4 v[52:55], v[8:15], v[230:237], v[52:55]
	v_mfma_f32_16x16x128_f8f6f4 v[44:47], v[0:7], v[230:237], v[44:47]
	v_mfma_f32_16x16x128_f8f6f4 v[36:39], v[8:15], v[238:245], v[36:39]
	v_mfma_f32_16x16x128_f8f6f4 v[32:35], v[0:7], v[238:245], v[32:35]
	s_setprio 0
	s_barrier
	ds_read_b128 v[0:3], v252 offset:32768
	ds_read_b128 v[4:7], v253 offset:32768
	ds_read_b128 v[8:11], v252 offset:34816
	ds_read_b128 v[12:15], v253 offset:34816
	ds_read_b128 v[16:19], v252 offset:49152
	ds_read_b128 v[20:23], v253 offset:49152
	ds_read_b128 v[24:27], v252 offset:51200
	ds_read_b128 v[28:31], v253 offset:51200
	s_mov_b32 m0, s37
	ds_read_b128 v[214:217], v206 offset:32768
	ds_read_b128 v[222:225], v206 offset:34816
	ds_read_b128 v[218:221], v207 offset:32768
	ds_read_b128 v[226:229], v207 offset:34816
	ds_read_b128 v[230:233], v206 offset:36864
	ds_read_b128 v[238:241], v206 offset:38912
	ds_read_b128 v[234:237], v207 offset:36864
	ds_read_b128 v[242:245], v207 offset:38912
	global_load_lds_dwordx4 v184, s[26:27]
	s_mov_b32 m0, s38
	s_nop 0
	global_load_lds_dwordx4 v182, s[26:27]
	s_waitcnt vmcnt(8)
	s_waitcnt lgkmcnt(0)
	s_barrier
	s_setprio 1
	s_waitcnt lgkmcnt(0)
	v_mfma_f32_16x16x128_f8f6f4 v[156:159], v[0:7], v[214:221], v[156:159]
	v_mfma_f32_16x16x128_f8f6f4 v[152:155], v[8:15], v[214:221], v[152:155]
	v_mfma_f32_16x16x128_f8f6f4 v[144:147], v[0:7], v[222:229], v[144:147]
	v_mfma_f32_16x16x128_f8f6f4 v[136:139], v[8:15], v[222:229], v[136:139]
	v_mfma_f32_16x16x128_f8f6f4 v[124:127], v[0:7], v[230:237], v[124:127]
	v_mfma_f32_16x16x128_f8f6f4 v[120:123], v[8:15], v[230:237], v[120:123]
	v_mfma_f32_16x16x128_f8f6f4 v[112:115], v[0:7], v[238:245], v[112:115]
	v_mfma_f32_16x16x128_f8f6f4 v[104:107], v[8:15], v[238:245], v[104:107]
	v_mfma_f32_16x16x128_f8f6f4 v[148:151], v[16:23], v[214:221], v[148:151]
	v_mfma_f32_16x16x128_f8f6f4 v[140:143], v[24:31], v[214:221], v[140:143]
	v_mfma_f32_16x16x128_f8f6f4 v[132:135], v[16:23], v[222:229], v[132:135]
	v_mfma_f32_16x16x128_f8f6f4 v[128:131], v[24:31], v[222:229], v[128:131]
	v_mfma_f32_16x16x128_f8f6f4 v[116:119], v[16:23], v[230:237], v[116:119]
	v_mfma_f32_16x16x128_f8f6f4 v[108:111], v[24:31], v[230:237], v[108:111]
	v_mfma_f32_16x16x128_f8f6f4 v[100:103], v[16:23], v[238:245], v[100:103]
	v_mfma_f32_16x16x128_f8f6f4 v[96:99], v[24:31], v[238:245], v[96:99]
	s_setprio 0
	s_barrier
	s_add_i32 s99, s34, 0x17f80
	s_mov_b32 m0, s99
	ds_read_b128 v[214:217], v206 offset:49152
	ds_read_b128 v[222:225], v206 offset:51200
	ds_read_b128 v[218:221], v207 offset:49152
	ds_read_b128 v[226:229], v207 offset:51200
	ds_read_b128 v[230:233], v206 offset:53248
	ds_read_b128 v[238:241], v206 offset:55296
	ds_read_b128 v[234:237], v207 offset:53248
	ds_read_b128 v[242:245], v207 offset:55296
	global_load_lds_dwordx4 v160, s[28:29] offset:128
	s_add_i32 m0, s99, 0x2000
	s_add_i32 s99, s34, 0x1bf80
	global_load_lds_dwordx4 v162, s[28:29] offset:128
	s_mov_b32 m0, s99
	s_nop 0
	global_load_lds_dwordx4 v160, s[30:31] offset:128
	s_add_i32 m0, s99, 0x2000
	s_nop 0
	global_load_lds_dwordx4 v162, s[30:31] offset:128
	s_add_i32 m0, s41, 0xffffff80
	s_nop 0
	global_load_lds_dwordx4 v164, s[26:27] offset:128
	s_add_i32 m0, s42, 0xffffff80
	s_nop 0
	global_load_lds_dwordx4 v166, s[26:27] offset:128
	s_waitcnt vmcnt(8)
	s_waitcnt lgkmcnt(0)
	s_barrier
	s_setprio 1
	s_waitcnt lgkmcnt(0)
	v_mfma_f32_16x16x128_f8f6f4 v[92:95], v[0:7], v[214:221], v[92:95]
	v_mfma_f32_16x16x128_f8f6f4 v[88:91], v[8:15], v[214:221], v[88:91]
	v_mfma_f32_16x16x128_f8f6f4 v[80:83], v[0:7], v[222:229], v[80:83]
	v_mfma_f32_16x16x128_f8f6f4 v[72:75], v[8:15], v[222:229], v[72:75]
	v_mfma_f32_16x16x128_f8f6f4 v[60:63], v[0:7], v[230:237], v[60:63]
	v_mfma_f32_16x16x128_f8f6f4 v[56:59], v[8:15], v[230:237], v[56:59]
	v_mfma_f32_16x16x128_f8f6f4 v[48:51], v[0:7], v[238:245], v[48:51]
	v_mfma_f32_16x16x128_f8f6f4 v[40:43], v[8:15], v[238:245], v[40:43]
	v_mfma_f32_16x16x128_f8f6f4 v[84:87], v[16:23], v[214:221], v[84:87]
	v_mfma_f32_16x16x128_f8f6f4 v[76:79], v[24:31], v[214:221], v[76:79]
	v_mfma_f32_16x16x128_f8f6f4 v[68:71], v[16:23], v[222:229], v[68:71]
	v_mfma_f32_16x16x128_f8f6f4 v[64:67], v[24:31], v[222:229], v[64:67]
	v_mfma_f32_16x16x128_f8f6f4 v[52:55], v[16:23], v[230:237], v[52:55]
	v_mfma_f32_16x16x128_f8f6f4 v[44:47], v[24:31], v[230:237], v[44:47]
	v_mfma_f32_16x16x128_f8f6f4 v[36:39], v[16:23], v[238:245], v[36:39]
	v_mfma_f32_16x16x128_f8f6f4 v[32:35], v[24:31], v[238:245], v[32:35]
	s_setprio 0
	s_barrier
	s_add_i32 s62, s62, 2
	s_add_u32 s24, s24, 0x100
	s_addc_u32 s25, s25, 0
	s_cmp_gt_u32 s62, 29
	s_cbranch_scc1 .LBB0_1552

	.amdhsa_kernel _Z6mk_fwd4Args
		.amdhsa_group_segment_fixed_size 0
		.amdhsa_private_segment_fixed_size 0
		.amdhsa_kernarg_size 528
		.amdhsa_user_sgpr_count 2
		.amdhsa_user_sgpr_dispatch_ptr 0
		.amdhsa_user_sgpr_queue_ptr 0
		.amdhsa_user_sgpr_kernarg_segment_ptr 1
		.amdhsa_user_sgpr_dispatch_id 0
		.amdhsa_user_sgpr_kernarg_preload_length 0
		.amdhsa_user_sgpr_kernarg_preload_offset 0
		.amdhsa_user_sgpr_private_segment_size 0
		.amdhsa_uses_dynamic_stack 0
		.amdhsa_enable_private_segment 0
		.amdhsa_system_sgpr_workgroup_id_x 1
		.amdhsa_system_sgpr_workgroup_id_y 0
		.amdhsa_system_sgpr_workgroup_id_z 0
		.amdhsa_system_sgpr_workgroup_info 0
		.amdhsa_system_vgpr_workitem_id 0
		.amdhsa_next_free_vgpr 256
		.amdhsa_next_free_sgpr 102
		.amdhsa_accum_offset 256
		.amdhsa_reserve_vcc 1
		.amdhsa_float_round_mode_32 0
		.amdhsa_float_round_mode_16_64 0
		.amdhsa_float_denorm_mode_32 3
		.amdhsa_float_denorm_mode_16_64 3
		.amdhsa_dx10_clamp 1
		.amdhsa_ieee_mode 1
		.amdhsa_fp16_overflow 0
		.amdhsa_tg_split 0
		.amdhsa_exception_fp_ieee_invalid_op 0
		.amdhsa_exception_fp_denorm_src 0
		.amdhsa_exception_fp_ieee_div_zero 0
		.amdhsa_exception_fp_ieee_overflow 0
		.amdhsa_exception_fp_ieee_underflow 0
		.amdhsa_exception_fp_ieee_inexact 0
		.amdhsa_exception_int_div_zero 0
	.end_amdhsa_kernel

amdhsa.kernels:
  - .agpr_count:     0
    .args:
      - .offset:         0
        .size:           272
        .value_kind:     by_value
      - .offset:         272
        .size:           4
        .value_kind:     hidden_block_count_x
      - .offset:         276
        .size:           4
        .value_kind:     hidden_block_count_y
      - .offset:         280
        .size:           4
        .value_kind:     hidden_block_count_z
      - .offset:         284
        .size:           2
        .value_kind:     hidden_group_size_x
      - .offset:         286
        .size:           2
        .value_kind:     hidden_group_size_y
      - .offset:         288
        .size:           2
        .value_kind:     hidden_group_size_z
      - .offset:         290
        .size:           2
        .value_kind:     hidden_remainder_x
      - .offset:         292
        .size:           2
        .value_kind:     hidden_remainder_y
      - .offset:         294
        .size:           2
        .value_kind:     hidden_remainder_z
      - .offset:         312
        .size:           8
        .value_kind:     hidden_global_offset_x
      - .offset:         320
        .size:           8
        .value_kind:     hidden_global_offset_y
      - .offset:         328
        .size:           8
        .value_kind:     hidden_global_offset_z
      - .offset:         336
        .size:           2
        .value_kind:     hidden_grid_dims
      - .offset:         392
        .size:           4
        .value_kind:     hidden_dynamic_lds_size
    .group_segment_fixed_size: 0
    .kernarg_segment_align: 8
    .kernarg_segment_size: 528
    .language:       OpenCL C
    .language_version:
      - 2
      - 0
    .max_flat_workgroup_size: 512
    .name:           _Z6mk_fwd4Args
    .private_segment_fixed_size: 0
    .sgpr_count:     108
    .sgpr_spill_count: 80
    .symbol:         _Z6mk_fwd4Args.kd
    .uniform_work_group_size: 1
    .uses_dynamic_stack: false
    .vgpr_count:     256
    .vgpr_spill_count: 0
    .wavefront_size: 64
